# speedup vs baseline: 1.0045x; 1.0045x over previous
.LBB4_26:
	s_or_b64 exec, exec, s[2:3]
	v_mov_b32_e32 v2, 0x10400
	ds_read_b128 v[2:5], v2
	v_mov_b32_e32 v6, 0x10410
	ds_read_b128 v[6:9], v6
	s_load_dwordx2 s[8:9], s[0:1], 0x80
	s_load_dwordx2 s[96:97], s[0:1], 0x90
	v_cmp_gt_u32_e32 vcc, 8, v0
	s_waitcnt lgkmcnt(0)
	v_and_b32_e32 v107, 15, v0
	v_lshlrev_b32_e32 v107, 4, v107
	v_mul_u32_u24_e32 v110, 5, v107
	global_load_dwordx4 v[112:115], v107, s[4:5]
	global_load_dwordx4 v[116:119], v110, s[96:97]
	global_load_dwordx4 v[120:123], v110, s[96:97] offset:16
	global_load_dwordx4 v[124:127], v110, s[96:97] offset:32
	global_load_dwordx4 v[128:131], v110, s[96:97] offset:48
	global_load_dwordx4 v[132:135], v110, s[96:97] offset:64
	v_cmp_eq_u32_e64 s[2:3], v2, v0
	s_nop 1
	v_cndmask_b32_e64 v2, 0, 1.0, s[2:3]
	v_cmp_eq_u32_e64 s[2:3], v3, v0
	s_nop 1
	v_cndmask_b32_e64 v3, 0, 1.0, s[2:3]
	v_cmp_eq_u32_e64 s[2:3], v4, v0
	v_add_f32_e32 v2, v2, v3
	s_nop 0
	v_cndmask_b32_e64 v3, 0, 1.0, s[2:3]
	v_cmp_eq_u32_e64 s[2:3], v5, v0
	v_add_f32_e32 v2, v2, v3
	s_nop 0
	v_cndmask_b32_e64 v3, 0, 1.0, s[2:3]
	v_cmp_eq_u32_e64 s[2:3], v6, v0
	v_add_f32_e32 v2, v2, v3
	s_nop 0
	v_cndmask_b32_e64 v3, 0, 1.0, s[2:3]
	v_cmp_eq_u32_e64 s[2:3], v7, v0
	v_add_f32_e32 v2, v2, v3
	s_nop 0
	v_cndmask_b32_e64 v3, 0, 1.0, s[2:3]
	v_cmp_eq_u32_e64 s[2:3], v8, v0
	v_add_f32_e32 v2, v2, v3
	s_nop 0
	v_cndmask_b32_e64 v3, 0, 1.0, s[2:3]
	v_add_f32_e32 v6, v2, v3
	v_mov_b32_e32 v2, 0x10420
	ds_read_b128 v[2:5], v2
	v_cmp_eq_u32_e64 s[2:3], v9, v0
	s_nop 1
	v_cndmask_b32_e64 v7, 0, 1.0, s[2:3]
	v_add_f32_e32 v10, v6, v7
	v_mov_b32_e32 v6, 0x10430
	ds_read_b128 v[6:9], v6
	s_waitcnt lgkmcnt(1)
	v_cmp_eq_u32_e64 s[2:3], v2, v0
	s_nop 1
	v_cndmask_b32_e64 v2, 0, 1.0, s[2:3]
	v_cmp_eq_u32_e64 s[2:3], v3, v0
	v_add_f32_e32 v2, v10, v2
	s_nop 0
	v_cndmask_b32_e64 v3, 0, 1.0, s[2:3]
	v_cmp_eq_u32_e64 s[2:3], v4, v0
	v_add_f32_e32 v2, v2, v3
	s_nop 0
	v_cndmask_b32_e64 v3, 0, 1.0, s[2:3]
	v_cmp_eq_u32_e64 s[2:3], v5, v0
	v_add_f32_e32 v2, v2, v3
	s_nop 0
	v_cndmask_b32_e64 v3, 0, 1.0, s[2:3]
	s_waitcnt lgkmcnt(0)
	v_cmp_eq_u32_e64 s[2:3], v6, v0
	v_add_f32_e32 v2, v2, v3
	s_nop 0
	v_cndmask_b32_e64 v3, 0, 1.0, s[2:3]
	v_cmp_eq_u32_e64 s[2:3], v7, v0
	v_add_f32_e32 v2, v2, v3
	s_nop 0
	v_cndmask_b32_e64 v3, 0, 1.0, s[2:3]
	v_cmp_eq_u32_e64 s[2:3], v8, v0
	v_add_f32_e32 v2, v2, v3
	s_nop 0
	v_cndmask_b32_e64 v3, 0, 1.0, s[2:3]
	v_add_f32_e32 v6, v2, v3
	v_mov_b32_e32 v2, 0x10440
	ds_read_b128 v[2:5], v2
	v_cmp_eq_u32_e64 s[2:3], v9, v0
	s_nop 1
	v_cndmask_b32_e64 v7, 0, 1.0, s[2:3]
	v_add_f32_e32 v10, v6, v7
	v_mov_b32_e32 v6, 0x10450
	ds_read_b128 v[6:9], v6
	s_waitcnt lgkmcnt(1)
	v_cmp_eq_u32_e64 s[2:3], v2, v0
	s_nop 1
	v_cndmask_b32_e64 v2, 0, 1.0, s[2:3]
	v_cmp_eq_u32_e64 s[2:3], v3, v0
	v_add_f32_e32 v2, v10, v2
	s_nop 0
	v_cndmask_b32_e64 v3, 0, 1.0, s[2:3]
	v_cmp_eq_u32_e64 s[2:3], v4, v0
	v_add_f32_e32 v2, v2, v3
	s_nop 0
	v_cndmask_b32_e64 v3, 0, 1.0, s[2:3]
	v_cmp_eq_u32_e64 s[2:3], v5, v0
	v_add_f32_e32 v2, v2, v3
	s_nop 0
	v_cndmask_b32_e64 v3, 0, 1.0, s[2:3]
	s_waitcnt lgkmcnt(0)
	v_cmp_eq_u32_e64 s[2:3], v6, v0
	v_add_f32_e32 v2, v2, v3
	s_nop 0
	v_cndmask_b32_e64 v3, 0, 1.0, s[2:3]
	v_cmp_eq_u32_e64 s[2:3], v7, v0
	v_add_f32_e32 v2, v2, v3
	s_nop 0
	v_cndmask_b32_e64 v3, 0, 1.0, s[2:3]
	v_cmp_eq_u32_e64 s[2:3], v8, v0
	v_add_f32_e32 v2, v2, v3
	s_nop 0
	v_cndmask_b32_e64 v3, 0, 1.0, s[2:3]
	v_add_f32_e32 v6, v2, v3
	v_mov_b32_e32 v2, 0x10460
	ds_read_b128 v[2:5], v2
	v_cmp_eq_u32_e64 s[2:3], v9, v0
	s_nop 1
	v_cndmask_b32_e64 v7, 0, 1.0, s[2:3]
	v_add_f32_e32 v10, v6, v7
	v_mov_b32_e32 v6, 0x10470
	ds_read_b128 v[6:9], v6
	s_waitcnt lgkmcnt(1)
	v_cmp_eq_u32_e64 s[2:3], v2, v0
	s_nop 1
	v_cndmask_b32_e64 v2, 0, 1.0, s[2:3]
	v_cmp_eq_u32_e64 s[2:3], v3, v0
	v_add_f32_e32 v2, v10, v2
	s_nop 0
	v_cndmask_b32_e64 v3, 0, 1.0, s[2:3]
	v_cmp_eq_u32_e64 s[2:3], v4, v0
	v_add_f32_e32 v2, v2, v3
	s_nop 0
	v_cndmask_b32_e64 v3, 0, 1.0, s[2:3]
	v_cmp_eq_u32_e64 s[2:3], v5, v0
	v_add_f32_e32 v2, v2, v3
	s_nop 0
	v_cndmask_b32_e64 v3, 0, 1.0, s[2:3]
	s_waitcnt lgkmcnt(0)
	v_cmp_eq_u32_e64 s[2:3], v6, v0
	v_add_f32_e32 v2, v2, v3
	s_nop 0
	v_cndmask_b32_e64 v3, 0, 1.0, s[2:3]
	v_cmp_eq_u32_e64 s[2:3], v7, v0
	v_add_f32_e32 v2, v2, v3
	s_nop 0
	v_cndmask_b32_e64 v3, 0, 1.0, s[2:3]
	v_cmp_eq_u32_e64 s[2:3], v8, v0
	v_add_f32_e32 v2, v2, v3
	s_nop 0
	v_cndmask_b32_e64 v3, 0, 1.0, s[2:3]
	v_cmp_eq_u32_e64 s[2:3], v9, v0
	v_add_f32_e32 v2, v2, v3
	s_nop 0
	v_cndmask_b32_e64 v3, 0, 1.0, s[2:3]
	v_add_f32_e32 v2, v2, v3
	v_cmp_neq_f32_e64 s[2:3], 0, v2
	s_and_b64 s[10:11], vcc, s[2:3]
	s_and_saveexec_b64 s[2:3], s[10:11]
	s_cbranch_execz .LBB4_28
	v_lshlrev_b32_e32 v4, 2, v0
	v_mov_b32_e32 v5, 0
	v_lshl_add_u64 v[4:5], s[6:7], 0, v[4:5]
	v_add_co_u32_e32 v4, vcc, 0x2000, v4
	s_nop 1
	v_addc_co_u32_e32 v5, vcc, 0, v5, vcc
	global_atomic_add_f32 v[4:5], v2, off
.LBB4_28:
	s_or_b64 exec, exec, s[2:3]
	s_bfe_u32 s6, s84, 0x10006
	s_lshr_b32 s7, s84, 7
	s_lshl_b32 s11, s7, 2
	s_lshl_b32 s10, s6, 4
	v_lshlrev_b32_e32 v18, 4, v1
	s_mov_b32 s3, 0
	v_mov_b32_e32 v19, 0
	s_add_i32 s2, s11, s10
	v_lshl_add_u64 v[6:7], s[8:9], 0, v[18:19]
	s_lshl_b64 s[8:9], s[2:3], 10
	v_lshl_add_u64 v[2:3], v[6:7], 0, s[8:9]
	global_load_dwordx4 v[22:25], v[2:3], off
	v_and_b32_e32 v1, 31, v0
	v_and_b32_e32 v2, 32, v0
	s_movk_i32 s2, 0x410
	s_or_b32 s12, s11, 1
	v_mad_u32_u24 v8, v1, s2, v2
	s_add_i32 s2, s12, s10
	s_lshl_b64 s[8:9], s[2:3], 10
	v_lshl_add_u64 v[2:3], v[6:7], 0, s[8:9]
	global_load_dwordx4 v[26:29], v[2:3], off
	s_or_b32 s2, s11, 2
	v_lshl_add_u32 v10, s2, 6, v8
	s_add_i32 s2, s2, s10
	v_lshl_add_u32 v4, s7, 8, v8
	s_or_b32 s11, s11, 3
	v_lshl_add_u32 v9, s12, 6, v8
	s_lshl_b64 s[8:9], s[2:3], 10
	ds_read_b128 v[30:33], v4
	ds_read_b128 v[2:5], v4 offset:16
	v_lshl_add_u32 v11, s11, 6, v8
	ds_read_b128 v[34:37], v9
	ds_read_b128 v[38:41], v9 offset:16
	ds_read_b128 v[42:45], v10
	ds_read_b128 v[46:49], v10 offset:16
	v_lshl_add_u64 v[8:9], v[6:7], 0, s[8:9]
	global_load_dwordx4 v[54:57], v[8:9], off
	s_add_i32 s2, s11, s10
	s_lshl_b64 s[2:3], s[2:3], 10
	ds_read_b128 v[58:61], v11
	ds_read_b128 v[62:65], v11 offset:16
	v_lshl_add_u64 v[10:11], v[6:7], 0, s[2:3]
	global_load_dwordx4 v[70:73], v[10:11], off
	s_waitcnt lgkmcnt(7)
	v_cvt_f16_f32_e32 v16, v30
	v_cvt_f16_f32_e32 v17, v31
	v_cvt_pk_f16_f32 v7, v32, v33
	s_waitcnt lgkmcnt(6)
	v_cvt_pk_f16_f32 v8, v2, v3
	v_cvt_pk_f16_f32 v9, v4, v5
	v_cvt_pk_f16_f32 v6, v30, v31
	v_cvt_f32_f16_e32 v10, v7
	v_cvt_f32_f16_sdwa v11, v7 dst_sel:DWORD dst_unused:UNUSED_PAD src0_sel:WORD_1
	v_cvt_f32_f16_e32 v12, v8
	v_cvt_f32_f16_sdwa v13, v8 dst_sel:DWORD dst_unused:UNUSED_PAD src0_sel:WORD_1
	v_cvt_f32_f16_e32 v14, v9
	v_cvt_f32_f16_sdwa v15, v9 dst_sel:DWORD dst_unused:UNUSED_PAD src0_sel:WORD_1
	v_cvt_f32_f16_e32 v84, v16
	v_cvt_f32_f16_e32 v91, v17
	v_pk_add_f32 v[10:11], v[32:33], v[10:11] neg_lo:[0,1] neg_hi:[0,1]
	v_pk_add_f32 v[2:3], v[2:3], v[12:13] neg_lo:[0,1] neg_hi:[0,1]
	v_pk_add_f32 v[4:5], v[4:5], v[14:15] neg_lo:[0,1] neg_hi:[0,1]
	v_cvt_pk_f16_f32 v85, v10, v11
	v_cvt_pk_f16_f32 v86, v2, v3
	v_cvt_pk_f16_f32 v87, v4, v5
	v_sub_f32_e32 v30, v30, v84
	v_sub_f32_e32 v31, v31, v91
	v_cvt_pk_f16_f32 v84, v30, v31
	s_waitcnt lgkmcnt(5)
	v_cvt_f16_f32_e32 v18, v34
	v_cvt_f16_f32_e32 v21, v35
	v_cvt_pk_f16_f32 v74, v34, v35
	v_cvt_pk_f16_f32 v75, v36, v37
	s_waitcnt lgkmcnt(4)
	v_cvt_pk_f16_f32 v76, v38, v39
	v_cvt_pk_f16_f32 v77, v40, v41
	v_cvt_f32_f16_e32 v50, v75
	v_cvt_f32_f16_sdwa v51, v75 dst_sel:DWORD dst_unused:UNUSED_PAD src0_sel:WORD_1
	v_cvt_f32_f16_e32 v66, v76
	v_cvt_f32_f16_sdwa v67, v76 dst_sel:DWORD dst_unused:UNUSED_PAD src0_sel:WORD_1
	v_cvt_f32_f16_e32 v88, v77
	v_cvt_f32_f16_sdwa v89, v77 dst_sel:DWORD dst_unused:UNUSED_PAD src0_sel:WORD_1
	v_cvt_f32_f16_e32 v18, v18
	v_cvt_f32_f16_e32 v21, v21
	s_waitcnt lgkmcnt(3)
	v_cvt_f16_f32_e32 v53, v42
	v_pk_add_f32 v[32:33], v[40:41], v[88:89] neg_lo:[0,1] neg_hi:[0,1]
	v_sub_f32_e32 v18, v34, v18
	v_sub_f32_e32 v21, v35, v21
	v_cvt_f16_f32_e32 v69, v43
	v_cvt_pk_f16_f32 v78, v42, v43
	v_cvt_pk_f16_f32 v79, v44, v45
	s_waitcnt lgkmcnt(2)
	v_cvt_pk_f16_f32 v80, v46, v47
	v_cvt_pk_f16_f32 v81, v48, v49
	v_cvt_f32_f16_e32 v90, v79
	s_waitcnt vmcnt(3)
	v_mfma_f32_32x32x16_f16 v[2:17], v[6:9], v[22:25], 0
	v_cvt_f32_f16_sdwa v91, v79 dst_sel:DWORD dst_unused:UNUSED_PAD src0_sel:WORD_1
	v_cvt_f32_f16_e32 v30, v80
	v_cvt_f32_f16_sdwa v31, v80 dst_sel:DWORD dst_unused:UNUSED_PAD src0_sel:WORD_1
	s_waitcnt lgkmcnt(1)
	v_cvt_f16_f32_e32 v82, v58
	v_cvt_pk_f16_f32 v83, v60, v61
	v_cvt_f16_f32_e32 v92, v59
	s_lshl_b32 s2, s6, 7
	v_mfma_f32_32x32x16_f16 v[2:17], v[84:87], v[22:25], v[2:17]
	v_add_f32_e64 v22, v36, -v50
	v_add_f32_e64 v23, v37, -v51
	v_add_f32_e64 v24, v38, -v66
	v_add_f32_e64 v25, v39, -v67
	v_cvt_pk_f16_f32 v23, v22, v23
	v_cvt_pk_f16_f32 v24, v24, v25
	v_cvt_pk_f16_f32 v25, v32, v33
	v_cvt_pk_f16_f32 v22, v18, v21
	v_cvt_f32_f16_e32 v32, v81
	s_waitcnt vmcnt(2)
	v_mfma_f32_32x32x16_f16 v[2:17], v[74:77], v[26:29], v[2:17]
	v_cvt_f32_f16_sdwa v33, v81 dst_sel:DWORD dst_unused:UNUSED_PAD src0_sel:WORD_1
	v_cvt_f32_f16_e32 v18, v53
	v_cvt_f32_f16_e32 v21, v69
	s_waitcnt lgkmcnt(0)
	v_cvt_pk_f16_f32 v84, v62, v63
	v_cvt_pk_f16_f32 v85, v64, v65
	v_sub_f32_e32 v18, v42, v18
	v_sub_f32_e32 v21, v43, v21
	v_mfma_f32_32x32x16_f16 v[2:17], v[22:25], v[26:29], v[2:17]
	v_add_f32_e64 v22, v44, -v90
	v_add_f32_e64 v23, v45, -v91
	v_add_f32_e64 v24, v46, -v30
	v_add_f32_e64 v25, v47, -v31
	v_add_f32_e64 v26, v48, -v32
	v_add_f32_e64 v27, v49, -v33
	v_cvt_pk_f16_f32 v23, v22, v23
	v_cvt_pk_f16_f32 v24, v24, v25
	v_cvt_pk_f16_f32 v25, v26, v27
	v_cvt_pk_f16_f32 v22, v18, v21
	s_waitcnt vmcnt(1)
	v_mfma_f32_32x32x16_f16 v[2:17], v[78:81], v[54:57], v[2:17]
	v_cvt_f32_f16_e32 v28, v82
	v_cvt_f32_f16_e32 v26, v83
	v_cvt_f32_f16_sdwa v27, v83 dst_sel:DWORD dst_unused:UNUSED_PAD src0_sel:WORD_1
	v_cvt_pk_f16_f32 v82, v58, v59
	v_cvt_f32_f16_e32 v18, v92
	v_sub_f32_e32 v21, v58, v28
	v_cvt_f32_f16_e32 v28, v85
	v_mfma_f32_32x32x16_f16 v[2:17], v[22:25], v[54:57], v[2:17]
	v_add_f32_e64 v24, v60, -v26
	v_add_f32_e64 v25, v61, -v27
	v_cvt_f32_f16_e32 v26, v84
	v_cvt_f32_f16_sdwa v27, v84 dst_sel:DWORD dst_unused:UNUSED_PAD src0_sel:WORD_1
	v_cvt_f32_f16_sdwa v29, v85 dst_sel:DWORD dst_unused:UNUSED_PAD src0_sel:WORD_1
	v_sub_f32_e32 v18, v59, v18
	v_cvt_pk_f16_f32 v23, v24, v25
	v_pk_add_f32 v[24:25], v[62:63], v[26:27] neg_lo:[0,1] neg_hi:[0,1]
	s_waitcnt vmcnt(0)
	v_mfma_f32_32x32x16_f16 v[2:17], v[82:85], v[70:73], v[2:17]
	v_add_f32_e64 v26, v64, -v28
	v_add_f32_e64 v27, v65, -v29
	v_cvt_pk_f16_f32 v22, v21, v18
	v_cvt_pk_f16_f32 v24, v24, v25
	v_cvt_pk_f16_f32 v25, v26, v27
	v_lshrrev_b32_e32 v18, 3, v0
	v_and_b32_e32 v18, 4, v18
	v_lshl_or_b32 v21, s7, 5, v18
	v_mfma_f32_32x32x16_f16 v[2:17], v[22:25], v[70:73], v[2:17]
	v_lshl_or_b32 v18, v1, 2, s2
	s_movk_i32 s6, 0x104
	v_mad_u64_u32 v[22:23], s[2:3], v21, s6, v[18:19]
	v_add_u32_e32 v1, 0x8000, v22
	s_load_dwordx2 s[2:3], s[0:1], 0x90
	s_nop 6
	ds_write2_b32 v1, v2, v3 offset0:128 offset1:193
	v_add_u32_e32 v1, 0x8400, v22
	ds_write2_b32 v1, v4, v5 offset0:2 offset1:67
	v_add_u32_e32 v1, 0x8800, v22
	ds_write2_b32 v1, v6, v7 offset0:136 offset1:201
	v_add_u32_e32 v1, 0x8c00, v22
	ds_write2_b32 v1, v8, v9 offset0:10 offset1:75
	v_add_u32_e32 v1, 0x9000, v22
	ds_write2_b32 v1, v10, v11 offset0:144 offset1:209
	v_add_u32_e32 v1, 0x9400, v22
	ds_write2_b32 v1, v12, v13 offset0:18 offset1:83
	v_add_u32_e32 v1, 0x9800, v22
	ds_write2_b32 v1, v14, v15 offset0:152 offset1:217
	v_add_u32_e32 v1, 0x9c00, v22
	ds_write2_b32 v1, v16, v17 offset0:26 offset1:91
	v_and_b32_e32 v16, 15, v0
	v_lshlrev_b32_e32 v18, 4, v16
	s_waitcnt lgkmcnt(0)
	s_barrier
	v_mov_b32_e32 v0, v112
	v_or_b32_e32 v4, 0x8200, v18
	v_mad_u32_u24 v1, v20, s6, v4
	ds_read_b32 v2, v1
	ds_read_b32 v3, v1 offset:8320
	ds_read_b32 v5, v1 offset:16640
	ds_read_b32 v1, v1 offset:24960
	s_waitcnt lgkmcnt(3)
	v_add_f32_e32 v0, v0, v2
	s_waitcnt lgkmcnt(2)
	v_add_f32_e32 v0, v0, v3
	s_waitcnt lgkmcnt(1)
	v_add_f32_e32 v0, v0, v5
	s_waitcnt lgkmcnt(0)
	v_add_f32_e32 v21, v0, v1
	v_mul_f32_e32 v17, 0x3f3504f3, v21
	v_cmp_nlt_f32_e64 s[6:7], |v17|, 1.0
	s_and_saveexec_b64 s[8:9], s[6:7]
	s_xor_b64 s[6:7], exec, s[8:9]
	s_cbranch_execz .LBB4_30
	s_mov_b32 s8, 0x378e98ab
	v_mov_b32_e32 v0, 0xb9c68948
	v_fma_f32 v0, |v17|, s8, v0
	s_mov_b32 s8, 0x3b7cd369
	v_fma_f32 v0, |v17|, v0, s8
	s_mov_b32 s8, 0xbcc618b2
	v_fma_f32 v0, |v17|, v0, s8
	s_mov_b32 s8, 0x3dda74e4
	v_fma_f32 v0, |v17|, v0, s8
	s_mov_b32 s8, 0x3f228afd
	v_fma_f32 v0, |v17|, v0, s8
	s_mov_b32 s8, 0x3e03c728
	v_fma_f32 v0, |v17|, v0, s8
	v_fma_f32 v0, |v17|, v0, |v17|
	s_mov_b32 s8, 0xbfb8aa3b
	v_mul_f32_e32 v1, 0xbfb8aa3b, v0
	v_fma_f32 v2, v0, s8, -v1
	v_rndne_f32_e32 v3, v1
	v_fmamk_f32 v2, v0, 0xb2a5705f, v2
	v_sub_f32_e32 v1, v1, v3
	v_add_f32_e32 v1, v1, v2
	v_exp_f32_e32 v1, v1
	v_cvt_i32_f32_e32 v2, v3
	s_mov_b32 s8, 0x42ce8ed0
	v_cmp_nlt_f32_e32 vcc, s8, v0
	s_mov_b32 s8, 0xc2b17218
	v_ldexp_f32 v1, v1, v2
	v_cndmask_b32_e32 v1, 0, v1, vcc
	v_mov_b32_e32 v2, 0x7f800000
	v_cmp_ngt_f32_e32 vcc, s8, v0
	s_nop 1
	v_cndmask_b32_e32 v0, v2, v1, vcc
	v_sub_f32_e32 v22, 1.0, v0
.LBB4_30:
	s_or_saveexec_b64 s[6:7], s[6:7]
	v_lshl_add_u64 v[12:13], s[4:5], 0, v[18:19]
	v_mul_u32_u24_e32 v5, 0x104, v20
	s_xor_b64 exec, exec, s[6:7]
	v_mul_f32_e32 v0, v17, v17
	v_mov_b32_e32 v1, 0x3ba10414
	v_fmac_f32_e32 v1, 0xba1345e1, v0
	v_fmaak_f32 v1, v0, v1, 0xbcdac9b8
	v_fmaak_f32 v1, v0, v1, 0x3de703be
	v_fmaak_f32 v1, v0, v1, 0xbec09330
	v_fmaak_f32 v0, v0, v1, 0x3e0375d0
	v_fma_f32 v22, |v17|, v0, |v17|
	s_or_b64 exec, exec, s[6:7]
	v_mov_b32_e32 v6, v113
	v_mul_u32_u24_e32 v0, 20, v16
	v_lshlrev_b32_e32 v7, 2, v0
	v_mov_b32_e32 v18, v120
	v_mov_b32_e32 v0, v116
	v_mov_b32_e32 v1, v117
	v_mov_b32_e32 v2, v118
	v_mov_b32_e32 v3, v119
	v_add_u32_e32 v28, v4, v5
	ds_read_b32 v4, v28 offset:4
	ds_read_b32 v5, v28 offset:8324
	ds_read_b32 v7, v28 offset:16644
	ds_read_b32 v8, v28 offset:24964
	s_waitcnt lgkmcnt(3)
	v_add_f32_e32 v4, v6, v4
	s_waitcnt lgkmcnt(2)
	v_add_f32_e32 v4, v4, v5
	s_waitcnt lgkmcnt(1)
	v_add_f32_e32 v4, v4, v7
	s_waitcnt lgkmcnt(0)
	v_add_f32_e32 v23, v4, v8
	v_mul_f32_e32 v19, 0x3f3504f3, v23
	v_cmp_nlt_f32_e64 s[4:5], |v19|, 1.0
	s_and_saveexec_b64 s[6:7], s[4:5]
	s_xor_b64 s[4:5], exec, s[6:7]
	s_cbranch_execz .LBB4_34
	s_mov_b32 s6, 0x378e98ab
	v_mov_b32_e32 v4, 0xb9c68948
	v_fma_f32 v4, |v19|, s6, v4
	s_mov_b32 s6, 0x3b7cd369
	v_fma_f32 v4, |v19|, v4, s6
	s_mov_b32 s6, 0xbcc618b2
	v_fma_f32 v4, |v19|, v4, s6
	s_mov_b32 s6, 0x3dda74e4
	v_fma_f32 v4, |v19|, v4, s6
	s_mov_b32 s6, 0x3f228afd
	v_fma_f32 v4, |v19|, v4, s6
	s_mov_b32 s6, 0x3e03c728
	v_fma_f32 v4, |v19|, v4, s6
	v_fma_f32 v4, |v19|, v4, |v19|
	s_mov_b32 s6, 0xbfb8aa3b
	v_mul_f32_e32 v5, 0xbfb8aa3b, v4
	v_fma_f32 v6, v4, s6, -v5
	v_rndne_f32_e32 v7, v5
	v_fmamk_f32 v6, v4, 0xb2a5705f, v6
	v_sub_f32_e32 v5, v5, v7
	v_add_f32_e32 v5, v5, v6
	v_exp_f32_e32 v5, v5
	v_cvt_i32_f32_e32 v6, v7
	s_mov_b32 s6, 0x42ce8ed0
	v_cmp_nlt_f32_e32 vcc, s6, v4
	s_mov_b32 s6, 0xc2b17218
	v_ldexp_f32 v5, v5, v6
	v_cndmask_b32_e32 v5, 0, v5, vcc
	v_mov_b32_e32 v6, 0x7f800000
	v_cmp_ngt_f32_e32 vcc, s6, v4
	s_nop 1
	v_cndmask_b32_e32 v4, v6, v5, vcc
	v_sub_f32_e32 v24, 1.0, v4
.LBB4_34:
	s_or_saveexec_b64 s[4:5], s[4:5]
	v_lshlrev_b32_e32 v4, 2, v16
	s_xor_b64 exec, exec, s[4:5]
	v_mul_f32_e32 v5, v19, v19
	v_mov_b32_e32 v6, 0x3ba10414
	v_fmac_f32_e32 v6, 0xba1345e1, v5
	v_fmaak_f32 v6, v5, v6, 0xbcdac9b8
	v_fmaak_f32 v6, v5, v6, 0x3de703be
	v_fmaak_f32 v6, v5, v6, 0xbec09330
	v_fmaak_f32 v5, v5, v6, 0x3e0375d0
	v_fma_f32 v24, |v19|, v5, |v19|
	s_or_b64 exec, exec, s[4:5]
	v_mov_b32_e32 v10, v114
	v_or_b32_e32 v4, 1, v4
	v_mul_u32_u24_e32 v4, 5, v4
	v_lshlrev_b32_e32 v8, 2, v4
	v_mov_b32_e32 v25, v125
	v_mov_b32_e32 v4, v121
	v_mov_b32_e32 v5, v122
	v_mov_b32_e32 v6, v123
	v_mov_b32_e32 v7, v124
	ds_read_b32 v11, v28 offset:8
	ds_read_b32 v14, v28 offset:8328
	ds_read_b32 v15, v28 offset:16648
	ds_read_b32 v26, v28 offset:24968
	v_mov_b32_e32 v9, 0
	s_waitcnt lgkmcnt(3)
	v_add_f32_e32 v10, v10, v11
	s_waitcnt lgkmcnt(2)
	v_add_f32_e32 v10, v10, v14
	s_waitcnt lgkmcnt(1)
	v_add_f32_e32 v10, v10, v15
	s_waitcnt lgkmcnt(0)
	v_add_f32_e32 v27, v10, v26
	v_mul_f32_e32 v26, 0x3f3504f3, v27
	v_cmp_nlt_f32_e64 s[4:5], |v26|, 1.0
	s_and_saveexec_b64 s[6:7], s[4:5]
	s_xor_b64 s[4:5], exec, s[6:7]
	s_cbranch_execz .LBB4_38
	s_mov_b32 s6, 0x378e98ab
	v_mov_b32_e32 v10, 0xb9c68948
	v_fma_f32 v10, |v26|, s6, v10
	s_mov_b32 s6, 0x3b7cd369
	v_fma_f32 v10, |v26|, v10, s6
	s_mov_b32 s6, 0xbcc618b2
	v_fma_f32 v10, |v26|, v10, s6
	s_mov_b32 s6, 0x3dda74e4
	v_fma_f32 v10, |v26|, v10, s6
	s_mov_b32 s6, 0x3f228afd
	v_fma_f32 v10, |v26|, v10, s6
	s_mov_b32 s6, 0x3e03c728
	v_fma_f32 v10, |v26|, v10, s6
	v_fma_f32 v10, |v26|, v10, |v26|
	s_mov_b32 s6, 0xbfb8aa3b
	v_mul_f32_e32 v11, 0xbfb8aa3b, v10
	v_fma_f32 v14, v10, s6, -v11
	v_rndne_f32_e32 v15, v11
	v_fmamk_f32 v14, v10, 0xb2a5705f, v14
	v_sub_f32_e32 v11, v11, v15
	v_add_f32_e32 v11, v11, v14
	v_exp_f32_e32 v11, v11
	v_cvt_i32_f32_e32 v14, v15
	s_mov_b32 s6, 0x42ce8ed0
	v_cmp_nlt_f32_e32 vcc, s6, v10
	s_mov_b32 s6, 0xc2b17218
	v_ldexp_f32 v11, v11, v14
	v_cndmask_b32_e32 v11, 0, v11, vcc
	v_mov_b32_e32 v14, 0x7f800000
	v_cmp_ngt_f32_e32 vcc, s6, v10
	s_nop 1
	v_cndmask_b32_e32 v10, v14, v11, vcc
	v_sub_f32_e32 v29, 1.0, v10
.LBB4_38:
	s_or_saveexec_b64 s[4:5], s[4:5]
	v_lshl_add_u64 v[14:15], s[2:3], 0, v[8:9]
	s_xor_b64 exec, exec, s[4:5]
	v_mul_f32_e32 v8, v26, v26
	v_mov_b32_e32 v9, 0x3ba10414
	v_fmac_f32_e32 v9, 0xba1345e1, v8
	v_fmaak_f32 v9, v8, v9, 0xbcdac9b8
	v_fmaak_f32 v9, v8, v9, 0x3de703be
	v_fmaak_f32 v9, v8, v9, 0xbec09330
	v_fmaak_f32 v8, v8, v9, 0x3e0375d0
	v_fma_f32 v29, |v26|, v8, |v26|
	s_or_b64 exec, exec, s[4:5]
	v_mov_b32_e32 v31, v115
	v_mov_b32_e32 v30, v130
	v_mov_b32_e32 v8, v126
	v_mov_b32_e32 v9, v127
	v_mov_b32_e32 v10, v128
	v_mov_b32_e32 v11, v129
	ds_read_b32 v12, v28 offset:12
	ds_read_b32 v13, v28 offset:8332
	ds_read_b32 v32, v28 offset:16652
	ds_read_b32 v28, v28 offset:24972
	s_waitcnt lgkmcnt(3)
	v_add_f32_e32 v12, v31, v12
	s_waitcnt lgkmcnt(2)
	v_add_f32_e32 v12, v12, v13
	s_waitcnt lgkmcnt(1)
	v_add_f32_e32 v12, v12, v32
	s_waitcnt lgkmcnt(0)
	v_add_f32_e32 v13, v12, v28
	v_mul_f32_e32 v12, 0x3f3504f3, v13
	v_cmp_nlt_f32_e64 s[2:3], |v12|, 1.0
	s_and_saveexec_b64 s[4:5], s[2:3]
	s_xor_b64 s[2:3], exec, s[4:5]
	s_cbranch_execz .LBB4_42
	s_mov_b32 s4, 0x378e98ab
	v_mov_b32_e32 v28, 0xb9c68948
	v_fma_f32 v28, |v12|, s4, v28
	s_mov_b32 s4, 0x3b7cd369
	v_fma_f32 v28, |v12|, v28, s4
	s_mov_b32 s4, 0xbcc618b2
	v_fma_f32 v28, |v12|, v28, s4
	s_mov_b32 s4, 0x3dda74e4
	v_fma_f32 v28, |v12|, v28, s4
	s_mov_b32 s4, 0x3f228afd
	v_fma_f32 v28, |v12|, v28, s4
	s_mov_b32 s4, 0x3e03c728
	v_fma_f32 v28, |v12|, v28, s4
	v_fma_f32 v28, |v12|, v28, |v12|
	s_mov_b32 s4, 0xbfb8aa3b
	v_mul_f32_e32 v31, 0xbfb8aa3b, v28
	v_fma_f32 v32, v28, s4, -v31
	v_rndne_f32_e32 v33, v31
	v_fmamk_f32 v32, v28, 0xb2a5705f, v32
	v_sub_f32_e32 v31, v31, v33
	v_add_f32_e32 v31, v31, v32
	v_exp_f32_e32 v31, v31
	v_cvt_i32_f32_e32 v32, v33
	s_mov_b32 s4, 0x42ce8ed0
	v_cmp_nlt_f32_e32 vcc, s4, v28
	s_mov_b32 s4, 0xc2b17218
	v_ldexp_f32 v31, v31, v32
	v_cndmask_b32_e32 v31, 0, v31, vcc
	v_mov_b32_e32 v32, 0x7f800000
	v_cmp_ngt_f32_e32 vcc, s4, v28
	s_nop 1
	v_cndmask_b32_e32 v28, v32, v31, vcc
	v_sub_f32_e32 v28, 1.0, v28
.LBB4_42:
	s_andn2_saveexec_b64 s[2:3], s[2:3]
	v_mul_f32_e32 v28, v12, v12
	v_mov_b32_e32 v31, 0x3ba10414
	v_fmac_f32_e32 v31, 0xba1345e1, v28
	v_fmaak_f32 v31, v28, v31, 0xbcdac9b8
	v_fmaak_f32 v31, v28, v31, 0x3de703be
	v_fmaak_f32 v31, v28, v31, 0xbec09330
	v_fmaak_f32 v28, v28, v31, 0x3e0375d0
	v_fma_f32 v28, |v12|, v28, |v12|
	s_or_b64 exec, exec, s[2:3]
	v_mov_b32_e32 v31, v135
	v_mov_b32_e32 v32, v131
	v_mov_b32_e32 v33, v132
	v_mov_b32_e32 v34, v133
	v_mov_b32_e32 v35, v134
	s_brev_b32 s2, -2
	v_bfi_b32 v17, s2, v22, v17
	v_mul_f32_e32 v14, 0.5, v21
	v_mul_f32_e32 v15, 0.5, v23
	v_xor_b32_e32 v23, 1, v68
	v_bfi_b32 v19, s2, v24, v19
	v_bfi_b32 v12, s2, v28, v12
	v_add_f32_e32 v17, 1.0, v17
	v_mul_f32_e32 v13, 0.5, v13
	v_bfi_b32 v22, s2, v29, v26
	v_cmp_lt_i32_e32 vcc, v23, v52
	v_add_f32_e32 v19, 1.0, v19
	v_add_f32_e32 v24, 1.0, v12
	v_mul_f32_e32 v12, v14, v17
	v_mul_f32_e32 v21, 0.5, v27
	v_cndmask_b32_e32 v23, v68, v23, vcc
	v_add_f32_e32 v22, 1.0, v22
	v_mul_f32_e32 v14, v15, v19
	v_pk_fma_f32 v[0:1], v[12:13], v[0:1], 0 op_sel_hi:[0,1,0]
	v_pk_fma_f32 v[2:3], v[12:13], v[2:3], 0 op_sel_hi:[0,1,0]
	v_fma_f32 v12, v12, v18, 0
	v_lshlrev_b32_e32 v23, 2, v23
	v_mul_f32_e32 v22, v21, v22
	v_pk_fma_f32 v[0:1], v[14:15], v[4:5], v[0:1] op_sel_hi:[0,1,1]
	v_pk_fma_f32 v[2:3], v[14:15], v[6:7], v[2:3] op_sel_hi:[0,1,1]
	v_fmac_f32_e32 v12, v14, v25
	v_mul_f32_e32 v24, v13, v24
	v_pk_fma_f32 v[0:1], v[22:23], v[8:9], v[0:1] op_sel_hi:[0,1,1]
	v_pk_fma_f32 v[2:3], v[22:23], v[10:11], v[2:3] op_sel_hi:[0,1,1]
	v_fmac_f32_e32 v12, v22, v30
	v_xor_b32_e32 v27, 2, v68
	v_cmp_lt_i32_e32 vcc, v27, v52
	v_xor_b32_e32 v36, 4, v68
	v_xor_b32_e32 v37, 8, v68
	v_cndmask_b32_e32 v9, v68, v27, vcc
	v_lshlrev_b32_e32 v9, 2, v9
	v_cmp_lt_i32_e32 vcc, v36, v52
	v_fmac_f32_e32 v12, v24, v31
	v_pk_fma_f32 v[0:1], v[24:25], v[32:33], v[0:1] op_sel_hi:[0,1,1]
	v_pk_fma_f32 v[2:3], v[24:25], v[34:35], v[2:3] op_sel_hi:[0,1,1]
	ds_bpermute_b32 v4, v23, v0
	ds_bpermute_b32 v5, v23, v1
	ds_bpermute_b32 v6, v23, v2
	ds_bpermute_b32 v7, v23, v3
	ds_bpermute_b32 v8, v23, v12
	v_cndmask_b32_e32 v10, v68, v36, vcc
	s_waitcnt lgkmcnt(3)
	v_pk_add_f32 v[0:1], v[0:1], v[4:5]
	ds_bpermute_b32 v4, v9, v0
	s_waitcnt lgkmcnt(2)
	v_pk_add_f32 v[2:3], v[2:3], v[6:7]
	s_waitcnt lgkmcnt(1)
	v_add_f32_e32 v8, v12, v8
	ds_bpermute_b32 v5, v9, v1
	ds_bpermute_b32 v6, v9, v2
	ds_bpermute_b32 v7, v9, v3
	ds_bpermute_b32 v9, v9, v8
	v_lshlrev_b32_e32 v10, 2, v10
	s_waitcnt lgkmcnt(3)
	v_pk_add_f32 v[0:1], v[0:1], v[4:5]
	ds_bpermute_b32 v4, v10, v0
	s_waitcnt lgkmcnt(2)
	v_pk_add_f32 v[2:3], v[2:3], v[6:7]
	s_waitcnt lgkmcnt(1)
	v_add_f32_e32 v8, v8, v9
	ds_bpermute_b32 v5, v10, v1
	ds_bpermute_b32 v6, v10, v2
	ds_bpermute_b32 v7, v10, v3
	ds_bpermute_b32 v9, v10, v8
	v_cmp_lt_i32_e32 vcc, v37, v52
	s_waitcnt lgkmcnt(3)
	v_pk_add_f32 v[4:5], v[0:1], v[4:5]
	s_waitcnt lgkmcnt(1)
	v_pk_add_f32 v[0:1], v[2:3], v[6:7]
	v_cndmask_b32_e32 v10, v68, v37, vcc
	v_lshlrev_b32_e32 v10, 2, v10
	s_waitcnt lgkmcnt(0)
	v_add_f32_e32 v8, v8, v9
	ds_bpermute_b32 v6, v10, v4
	ds_bpermute_b32 v7, v10, v5
	ds_bpermute_b32 v2, v10, v0
	ds_bpermute_b32 v3, v10, v1
	ds_bpermute_b32 v9, v10, v8
	v_cmp_eq_u32_e32 vcc, 0, v16
	s_and_saveexec_b64 s[2:3], vcc
	s_cbranch_execz .LBB4_46
	s_load_dwordx4 s[0:3], s[0:1], 0x98
	s_waitcnt lgkmcnt(0)
	v_add_f32_e32 v8, v8, v9
	v_add_u32_e32 v9, s33, v20
	v_pk_add_f32 v[4:5], v[4:5], v[6:7]
	v_pk_add_f32 v[2:3], v[0:1], v[2:3]
	s_load_dwordx4 s[4:7], s[0:1], 0x0
	s_load_dword s8, s[0:1], 0x10
	v_mad_i64_i32 v[6:7], s[0:1], v9, 20, s[2:3]
	s_waitcnt lgkmcnt(0)
	v_pk_add_f32 v[0:1], v[4:5], s[4:5]
	v_pk_add_f32 v[2:3], v[2:3], s[6:7]
	global_store_dwordx4 v[6:7], v[0:3], off
	s_nop 1
	v_add_f32_e32 v0, s8, v8
	global_store_dword v[6:7], v0, off offset:16

	.amdhsa_kernel _Z9k_redprepILi2EEvPKfPKjS1_S1_S1_S1_S1_PfPKDv8_DF16_S7_S1_PDF16_S4_S4_S4_PKiS7_S1_S1_S1_S4_S4_
		.amdhsa_group_segment_fixed_size 66688
		.amdhsa_private_segment_fixed_size 0
		.amdhsa_kernarg_size 176
		.amdhsa_user_sgpr_count 2
		.amdhsa_user_sgpr_dispatch_ptr 0
		.amdhsa_user_sgpr_queue_ptr 0
		.amdhsa_user_sgpr_kernarg_segment_ptr 1
		.amdhsa_user_sgpr_dispatch_id 0
		.amdhsa_user_sgpr_kernarg_preload_length 0
		.amdhsa_user_sgpr_kernarg_preload_offset 0
		.amdhsa_user_sgpr_private_segment_size 0
		.amdhsa_uses_dynamic_stack 0
		.amdhsa_enable_private_segment 0
		.amdhsa_system_sgpr_workgroup_id_x 1
		.amdhsa_system_sgpr_workgroup_id_y 0
		.amdhsa_system_sgpr_workgroup_id_z 0
		.amdhsa_system_sgpr_workgroup_info 0
		.amdhsa_system_vgpr_workitem_id 0
		.amdhsa_next_free_vgpr 136
		.amdhsa_next_free_sgpr 98
		.amdhsa_accum_offset 136
		.amdhsa_reserve_vcc 1
		.amdhsa_float_round_mode_32 0
		.amdhsa_float_round_mode_16_64 0
		.amdhsa_float_denorm_mode_32 3
		.amdhsa_float_denorm_mode_16_64 3
		.amdhsa_dx10_clamp 1
		.amdhsa_ieee_mode 1
		.amdhsa_fp16_overflow 0
		.amdhsa_tg_split 0
		.amdhsa_exception_fp_ieee_invalid_op 0
		.amdhsa_exception_fp_denorm_src 0
		.amdhsa_exception_fp_ieee_div_zero 0
		.amdhsa_exception_fp_ieee_overflow 0
		.amdhsa_exception_fp_ieee_underflow 0
		.amdhsa_exception_fp_ieee_inexact 0
		.amdhsa_exception_int_div_zero 0
	.end_amdhsa_kernel

amdhsa.kernels:
  - .agpr_count:     0
    .args:
      - .actual_access:  read_only
        .address_space:  global
        .offset:         0
        .size:           8
        .value_kind:     global_buffer
      - .address_space:  global
        .offset:         8
        .size:           8
        .value_kind:     global_buffer
      - .actual_access:  read_only
        .address_space:  global
        .offset:         16
        .size:           8
        .value_kind:     global_buffer
      - .actual_access:  read_only
        .address_space:  global
        .offset:         24
        .size:           8
        .value_kind:     global_buffer
      - .actual_access:  read_only
        .address_space:  global
        .offset:         32
        .size:           8
        .value_kind:     global_buffer
      - .actual_access:  read_only
        .address_space:  global
        .offset:         40
        .size:           8
        .value_kind:     global_buffer
      - .actual_access:  read_only
        .address_space:  global
        .offset:         48
        .size:           8
        .value_kind:     global_buffer
      - .actual_access:  read_only
        .address_space:  global
        .offset:         56
        .size:           8
        .value_kind:     global_buffer
      - .actual_access:  write_only
        .address_space:  global
        .offset:         64
        .size:           8
        .value_kind:     global_buffer
      - .actual_access:  write_only
        .address_space:  global
        .offset:         72
        .size:           8
        .value_kind:     global_buffer
      - .actual_access:  write_only
        .address_space:  global
        .offset:         80
        .size:           8
        .value_kind:     global_buffer
      - .actual_access:  write_only
        .address_space:  global
        .offset:         88
        .size:           8
        .value_kind:     global_buffer
      - .actual_access:  read_only
        .address_space:  global
        .offset:         96
        .size:           8
        .value_kind:     global_buffer
      - .actual_access:  write_only
        .address_space:  global
        .offset:         104
        .size:           8
        .value_kind:     global_buffer
      - .actual_access:  read_only
        .address_space:  global
        .offset:         112
        .size:           8
        .value_kind:     global_buffer
      - .actual_access:  write_only
        .address_space:  global
        .offset:         120
        .size:           8
        .value_kind:     global_buffer
      - .actual_access:  write_only
        .address_space:  global
        .offset:         128
        .size:           8
        .value_kind:     global_buffer
      - .actual_access:  write_only
        .address_space:  global
        .offset:         136
        .size:           8
        .value_kind:     global_buffer
      - .actual_access:  write_only
        .address_space:  global
        .offset:         144
        .size:           8
        .value_kind:     global_buffer
    .group_segment_fixed_size: 4096
    .kernarg_segment_align: 8
    .kernarg_segment_size: 152
    .language:       OpenCL C
    .language_version:
      - 2
      - 0
    .max_flat_workgroup_size: 512
    .name:           _Z7k_frontPKfPmS0_S0_S0_S0_S0_S0_PDF16_S2_PfS3_S0_S2_S0_S2_S3_S3_S3_
    .private_segment_fixed_size: 0
    .sgpr_count:     88
    .sgpr_spill_count: 0
    .symbol:         _Z7k_frontPKfPmS0_S0_S0_S0_S0_S0_PDF16_S2_PfS3_S0_S2_S0_S2_S3_S3_S3_.kd
    .uniform_work_group_size: 1
    .uses_dynamic_stack: false
    .vgpr_count:     68
    .vgpr_spill_count: 0
    .wavefront_size: 64
  - .agpr_count:     256
    .args:
      - .actual_access:  read_only
        .address_space:  global
        .offset:         0
        .size:           8
        .value_kind:     global_buffer
      - .actual_access:  read_only
        .address_space:  global
        .offset:         8
        .size:           8
        .value_kind:     global_buffer
      - .actual_access:  read_only
        .address_space:  global
        .offset:         16
        .size:           8
        .value_kind:     global_buffer
      - .actual_access:  read_only
        .address_space:  global
        .offset:         24
        .size:           8
        .value_kind:     global_buffer
      - .actual_access:  read_only
        .address_space:  global
        .offset:         32
        .size:           8
        .value_kind:     global_buffer
      - .address_space:  global
        .offset:         40
        .size:           8
        .value_kind:     global_buffer
      - .actual_access:  write_only
        .address_space:  global
        .offset:         48
        .size:           8
        .value_kind:     global_buffer
      - .actual_access:  write_only
        .address_space:  global
        .offset:         56
        .size:           8
        .value_kind:     global_buffer
    .group_segment_fixed_size: 114688
    .kernarg_segment_align: 8
    .kernarg_segment_size: 64
    .language:       OpenCL C
    .language_version:
      - 2
      - 0
    .max_flat_workgroup_size: 256
    .name:           _Z6k_mainPKDF16_PKfS2_S2_PKmPjPfS6_
    .private_segment_fixed_size: 0
    .sgpr_count:     108
    .sgpr_spill_count: 0
    .symbol:         _Z6k_mainPKDF16_PKfS2_S2_PKmPjPfS6_.kd
    .uniform_work_group_size: 1
    .uses_dynamic_stack: false
    .vgpr_count:     492
    .vgpr_spill_count: 0
    .wavefront_size: 64
  - .agpr_count:     0
    .args:
      - .actual_access:  read_only
        .address_space:  global
        .offset:         0
        .size:           8
        .value_kind:     global_buffer
      - .actual_access:  read_only
        .address_space:  global
        .offset:         8
        .size:           8
        .value_kind:     global_buffer
      - .actual_access:  read_only
        .address_space:  global
        .offset:         16
        .size:           8
        .value_kind:     global_buffer
      - .actual_access:  read_only
        .address_space:  global
        .offset:         24
        .size:           8
        .value_kind:     global_buffer
      - .actual_access:  read_only
        .address_space:  global
        .offset:         32
        .size:           8
        .value_kind:     global_buffer
      - .actual_access:  read_only
        .address_space:  global
        .offset:         40
        .size:           8
        .value_kind:     global_buffer
      - .actual_access:  read_only
        .address_space:  global
        .offset:         48
        .size:           8
        .value_kind:     global_buffer
      - .actual_access:  read_only
        .address_space:  global
        .offset:         56
        .size:           8
        .value_kind:     global_buffer
      - .actual_access:  read_only
        .address_space:  global
        .offset:         64
        .size:           8
        .value_kind:     global_buffer
      - .actual_access:  write_only
        .address_space:  global
        .offset:         72
        .size:           8
        .value_kind:     global_buffer
      - .actual_access:  write_only
        .address_space:  global
        .offset:         80
        .size:           8
        .value_kind:     global_buffer
    .group_segment_fixed_size: 101632
    .kernarg_segment_align: 8
    .kernarg_segment_size: 88
    .language:       OpenCL C
    .language_version:
      - 2
      - 0
    .max_flat_workgroup_size: 256
    .name:           _Z7k_graphPKfS0_S0_S0_S0_S0_S0_S0_S0_PfS1_
    .private_segment_fixed_size: 0
    .sgpr_count:     25
    .sgpr_spill_count: 0
    .symbol:         _Z7k_graphPKfS0_S0_S0_S0_S0_S0_S0_S0_PfS1_.kd
    .uniform_work_group_size: 1
    .uses_dynamic_stack: false
    .vgpr_count:     236
    .vgpr_spill_count: 0
    .wavefront_size: 64
  - .agpr_count:     0
    .args:
      - .actual_access:  read_only
        .address_space:  global
        .offset:         0
        .size:           8
        .value_kind:     global_buffer
      - .actual_access:  read_only
        .address_space:  global
        .offset:         8
        .size:           8
        .value_kind:     global_buffer
      - .actual_access:  read_only
        .address_space:  global
        .offset:         16
        .size:           8
        .value_kind:     global_buffer
      - .actual_access:  read_only
        .address_space:  global
        .offset:         24
        .size:           8
        .value_kind:     global_buffer
      - .actual_access:  read_only
        .address_space:  global
        .offset:         32
        .size:           8
        .value_kind:     global_buffer
      - .actual_access:  read_only
        .address_space:  global
        .offset:         40
        .size:           8
        .value_kind:     global_buffer
      - .actual_access:  read_only
        .address_space:  global
        .offset:         48
        .size:           8
        .value_kind:     global_buffer
      - .address_space:  global
        .offset:         56
        .size:           8
        .value_kind:     global_buffer
      - .actual_access:  read_only
        .address_space:  global
        .offset:         64
        .size:           8
        .value_kind:     global_buffer
      - .actual_access:  read_only
        .address_space:  global
        .offset:         72
        .size:           8
        .value_kind:     global_buffer
      - .actual_access:  read_only
        .address_space:  global
        .offset:         80
        .size:           8
        .value_kind:     global_buffer
      - .address_space:  global
        .offset:         88
        .size:           8
        .value_kind:     global_buffer
      - .actual_access:  write_only
        .address_space:  global
        .offset:         96
        .size:           8
        .value_kind:     global_buffer
      - .actual_access:  write_only
        .address_space:  global
        .offset:         104
        .size:           8
        .value_kind:     global_buffer
      - .actual_access:  write_only
        .address_space:  global
        .offset:         112
        .size:           8
        .value_kind:     global_buffer
      - .actual_access:  read_only
        .address_space:  global
        .offset:         120
        .size:           8
        .value_kind:     global_buffer
      - .actual_access:  read_only
        .address_space:  global
        .offset:         128
        .size:           8
        .value_kind:     global_buffer
      - .actual_access:  read_only
        .address_space:  global
        .offset:         136
        .size:           8
        .value_kind:     global_buffer
      - .actual_access:  read_only
        .address_space:  global
        .offset:         144
        .size:           8
        .value_kind:     global_buffer
      - .actual_access:  read_only
        .address_space:  global
        .offset:         152
        .size:           8
        .value_kind:     global_buffer
      - .actual_access:  read_only
        .address_space:  global
        .offset:         160
        .size:           8
        .value_kind:     global_buffer
      - .actual_access:  read_only
        .address_space:  global
        .offset:         168
        .size:           8
        .value_kind:     global_buffer
    .group_segment_fixed_size: 53792
    .kernarg_segment_align: 8
    .kernarg_segment_size: 176
    .language:       OpenCL C
    .language_version:
      - 2
      - 0
    .max_flat_workgroup_size: 512
    .name:           _Z9k_redprepILi1EEvPKfPKjS1_S1_S1_S1_S1_PfPKDv8_DF16_S7_S1_PDF16_S4_S4_S4_PKiS7_S1_S1_S1_S4_S4_
    .private_segment_fixed_size: 0
    .sgpr_count:     106
    .sgpr_spill_count: 4
    .symbol:         _Z9k_redprepILi1EEvPKfPKjS1_S1_S1_S1_S1_PfPKDv8_DF16_S7_S1_PDF16_S4_S4_S4_PKiS7_S1_S1_S1_S4_S4_.kd
    .uniform_work_group_size: 1
    .uses_dynamic_stack: false
    .vgpr_count:     104
    .vgpr_spill_count: 0
    .wavefront_size: 64
  - .agpr_count:     0
    .args:
      - .actual_access:  read_only
        .address_space:  global
        .offset:         0
        .size:           8
        .value_kind:     global_buffer
      - .actual_access:  read_only
        .address_space:  global
        .offset:         8
        .size:           8
        .value_kind:     global_buffer
      - .actual_access:  read_only
        .address_space:  global
        .offset:         16
        .size:           8
        .value_kind:     global_buffer
      - .actual_access:  read_only
        .address_space:  global
        .offset:         24
        .size:           8
        .value_kind:     global_buffer
      - .actual_access:  read_only
        .address_space:  global
        .offset:         32
        .size:           8
        .value_kind:     global_buffer
      - .actual_access:  read_only
        .address_space:  global
        .offset:         40
        .size:           8
        .value_kind:     global_buffer
      - .actual_access:  read_only
        .address_space:  global
        .offset:         48
        .size:           8
        .value_kind:     global_buffer
      - .address_space:  global
        .offset:         56
        .size:           8
        .value_kind:     global_buffer
      - .actual_access:  read_only
        .address_space:  global
        .offset:         64
        .size:           8
        .value_kind:     global_buffer
      - .actual_access:  read_only
        .address_space:  global
        .offset:         72
        .size:           8
        .value_kind:     global_buffer
      - .actual_access:  read_only
        .address_space:  global
        .offset:         80
        .size:           8
        .value_kind:     global_buffer
      - .actual_access:  read_only
        .address_space:  global
        .offset:         88
        .size:           8
        .value_kind:     global_buffer
      - .actual_access:  read_only
        .address_space:  global
        .offset:         96
        .size:           8
        .value_kind:     global_buffer
      - .actual_access:  read_only
        .address_space:  global
        .offset:         104
        .size:           8
        .value_kind:     global_buffer
      - .actual_access:  read_only
        .address_space:  global
        .offset:         112
        .size:           8
        .value_kind:     global_buffer
      - .actual_access:  read_only
        .address_space:  global
        .offset:         120
        .size:           8
        .value_kind:     global_buffer
      - .actual_access:  read_only
        .address_space:  global
        .offset:         128
        .size:           8
        .value_kind:     global_buffer
      - .actual_access:  read_only
        .address_space:  global
        .offset:         136
        .size:           8
        .value_kind:     global_buffer
      - .actual_access:  read_only
        .address_space:  global
        .offset:         144
        .size:           8
        .value_kind:     global_buffer
      - .actual_access:  read_only
        .address_space:  global
        .offset:         152
        .size:           8
        .value_kind:     global_buffer
      - .actual_access:  write_only
        .address_space:  global
        .offset:         160
        .size:           8
        .value_kind:     global_buffer
      - .address_space:  global
        .offset:         168
        .size:           8
        .value_kind:     global_buffer
    .group_segment_fixed_size: 66688
    .kernarg_segment_align: 8
    .kernarg_segment_size: 176
    .language:       OpenCL C
    .language_version:
      - 2
      - 0
    .max_flat_workgroup_size: 512
    .name:           _Z9k_redprepILi2EEvPKfPKjS1_S1_S1_S1_S1_PfPKDv8_DF16_S7_S1_PDF16_S4_S4_S4_PKiS7_S1_S1_S1_S4_S4_
    .private_segment_fixed_size: 0
    .sgpr_count:     104
    .sgpr_spill_count: 0
    .symbol:         _Z9k_redprepILi2EEvPKfPKjS1_S1_S1_S1_S1_PfPKDv8_DF16_S7_S1_PDF16_S4_S4_S4_PKiS7_S1_S1_S1_S4_S4_.kd
    .uniform_work_group_size: 1
    .uses_dynamic_stack: false
    .vgpr_count:     136
    .vgpr_spill_count: 0
    .wavefront_size: 64
